# P0 weight items dealt so that a WG's 8 waves take 8 consecutive k-blocks of one n-block (1 KB contiguous bf16 writes per row) on top of router loop rewrite
# baseline (speedup 1.0000x reference)
; __device__ __forceinline__ CvtD cvt_decode(Frame& F, int it) {
;     const int l = it / CI_PER_LAYER; int r = it - l * CI_PER_LAYER;
;     unsigned char* lwp = F.ws + WS_W + (size_t)l * LW_BYTES;
;     if (r < CI_IN) { const int kb = r / 434, nb = r - kb * 434; int n0, row0;
;         if (nb < 242) { n0 = 32 * nb; row0 = n0; } else { n0 = 7728 + 32 * (nb - 242); row0 = Z_MG + 32 * (nb - 242); }
;         return cvt_desc(inp(F, I_WIN) + (size_t)l * DM * IN_COLS, IN_COLS, 64 * kb, n0, (bf16*)(lwp + LW_IN), DM, row0); }
;     r -= CI_IN;
;     if (r < 3 * CI_BRI) { const int bi = r / CI_BRI; r -= bi * CI_BRI; const int kb = r / 64, nb = r % 64;
;         return cvt_desc(inp(F, I_WBR) + ((size_t)l * 3 + bi) * BW * DM, DM, 64 * kb, 32 * nb, (bf16*)(lwp + LW_BR) + (size_t)bi * BW, 3 * BW, 32 * nb); }
;     r -= 3 * CI_BRI;
;     if (r < CI_OUT) { const int kb = r / 64, nb = r % 64; return cvt_desc(inp(F, I_WOUT) + (size_t)l * DM * DM, DM, 64 * kb, 32 * nb, (bf16*)(lwp + LW_OUT), DM, 32 * nb); }
;     r -= CI_OUT;
;     if (r < NE * CI_GU) { const int e = r / CI_GU; r -= e * CI_GU; const int kb = r / 64, nb = r % 64; const int n = 32 * nb; int row0;
;         if (n < DE) row0 = (n >> 7) * 256 + (n & 127); else row0 = ((n - DE) >> 7) * 256 + 128 + ((n - DE) & 127);
;         return cvt_desc(inp(F, I_WGU) + ((size_t)l * NE + e) * DM * 2048, 2048, 64 * kb, n, (bf16*)(lwp + LW_GU) + (size_t)e * 2048 * DM, DM, row0); }
;     r -= NE * CI_GU;
;     if (r < NE * CI_DN) { const int e = r / CI_DN; r -= e * CI_DN; const int kb = r / 64, nb = r % 64;
;         return cvt_desc(inp(F, I_WDN) + ((size_t)l * NE + e) * DE * DM, DM, 64 * kb, 32 * nb, (bf16*)(lwp + LW_DN) + (size_t)e * DM * DE, DE, 32 * nb); }
;     r -= NE * CI_DN;
;     if (r < CI_PGI) { const int kb = r / 64, nb = r % 64; return cvt_desc(inp(F, I_WPG) + (size_t)l * DM * DM, DM, 64 * kb, 32 * nb, (bf16*)(lwp + LW_PG), DM, 32 * nb); }
;     r -= CI_PGI;
;     if (r < CI_PL) { const int kb = r / 64, nb = r % 64; return cvt_desc(inp(F, I_WPLE) + (size_t)l * PLE * DM, DM, 64 * kb, 32 * nb, (bf16*)(lwp + LW_PLE), PLE, 32 * nb); }
;     r -= CI_PL;
;     if (r < 2 * CI_P1) { const int kv = r / CI_P1; r -= kv * CI_P1; const int kb = r / 4, nb = r % 4;
;         return cvt_desc(inp(F, I_PW1) + ((size_t)l * 2 + kv) * 2048 * 128, 128, 64 * kb, 32 * nb, (bf16*)(lwp + LW_PHI1) + (size_t)kv * 128 * 2048, 2048, 32 * nb); }
.LBB0_7:
	s_or_b64 exec, exec, s[4:5]
	s_load_dwordx2 s[4:5], s[0:1], 0xe0
	s_and_b32 s0, s22, 0xffffffc0
	v_writelane_b32 v249, s0, 4
	s_waitcnt lgkmcnt(0)
	s_cmp_lt_i32 s4, 1
	s_cselect_b64 s[0:1], -1, 0
	v_writelane_b32 v249, s4, 5
	s_cmp_gt_i32 s5, 0
	s_nop 0
	v_writelane_b32 v249, s5, 6
	s_cselect_b64 s[4:5], -1, 0
	s_and_b64 s[16:17], s[0:1], s[4:5]
	s_andn2_b64 vcc, exec, s[16:17]
	s_cbranch_vccnz .LBB0_148
	s_mov_b32 s0, -1
	s_lshl_b32 s12, s92, 3
	v_mbcnt_lo_u32_b32 v0, s0, 0
	v_mbcnt_hi_u32_b32 v0, s0, v0
	v_readlane_b32 s0, v249, 4
	s_nop 1
	v_add_u32_e32 v64, s0, v0
	s_add_i32 s0, 0, 0x231d8
	v_mov_b32_e32 v0, s0
	ds_read_b64 v[0:1], v0
	v_readfirstlane_b32 s0, v64
	s_ashr_i32 s13, s0, 6
	s_cmp_eq_u32 s52, 0x100
	s_cbranch_scc0 .Lmy_p0deal_skip
	s_and_b32 s100, s92, 0xc0
	s_lshl_b32 s100, s100, 3
	s_and_b32 s101, s92, 63
	s_or_b32 s100, s100, s101
	s_mul_i32 s101, s13, 63
	s_add_i32 s12, s100, s101
.Lmy_p0deal_skip:
	s_add_i32 s101, s13, s12
	s_add_i32 s0, s13, s12
	s_cmp_gt_i32 s0, 0x2288f
	s_waitcnt lgkmcnt(0)
	v_readfirstlane_b32 s28, v0
	v_readfirstlane_b32 s29, v1
	s_cbranch_scc1 .LBB0_95
	s_mul_hi_i32 s1, s0, 0x769a913
	s_lshr_b32 s4, s1, 31
	s_ashr_i32 s1, s1, 11
	s_add_i32 s4, s1, s4
	s_mul_i32 s20, s4, 0xfffeebb8
	s_add_i32 s20, s20, s0
	s_add_u32 s22, s28, 0x1000000
	s_addc_u32 s23, s29, 0
	s_ashr_i32 s5, s4, 31
	s_mul_i32 s6, s4, 0x11600000
	s_mul_hi_i32 s1, s4, 0x11600000
	s_add_u32 s18, s22, s6
	s_addc_u32 s19, s23, s1
	s_cmpk_gt_i32 s20, 0x363f
	s_cbranch_scc0 .LBB0_18
	s_cmpk_gt_u32 s20, 0x423f
	s_cbranch_scc0 .LBB0_19
	s_cmpk_gt_u32 s20, 0x4a3f
	s_cbranch_scc0 .LBB0_20
	s_cmpk_gt_u32 s20, 0xca3f
	s_cbranch_scc0 .LBB0_21
	s_cmp_gt_u32 s20, 0x10a3f
	s_cbranch_scc0 .LBB0_22
	s_cmp_gt_u32 s20, 0x1123f
	s_cbranch_scc0 .LBB0_23
	s_cmp_gt_u32 s20, 0x1133f
	s_cbranch_scc0 .LBB0_24
	s_cmp_gt_u32 s20, 0x1143f
	s_cbranch_scc0 .LBB0_25
	s_add_i32 s1, 0, 0x23178
	v_mov_b32_e32 v0, s1
	ds_read_b64 v[0:1], v0
	s_add_i32 s1, s20, 0xfffeebc0
	s_lshr_b32 s6, s1, 2
	s_lshl_b64 s[8:9], s[4:5], 16
	s_mov_b32 s7, 0
	s_waitcnt lgkmcnt(0)
	v_readfirstlane_b32 s1, v0
	v_readfirstlane_b32 s10, v1
	s_add_u32 s1, s1, s8
	s_addc_u32 s10, s10, s9
	s_lshl_b64 s[8:9], s[6:7], 15
	s_add_u32 s8, s1, s8
	s_addc_u32 s9, s10, s9
	s_lshl_b32 s0, s0, 5
	s_and_b32 s10, s0, 64
	s_and_b32 s11, s0, 32
	s_lshl_b64 s[0:1], s[6:7], 14
	s_add_u32 s0, s18, s0
	s_addc_u32 s1, s19, s1
	s_lshl_b32 s6, s10, 8
	s_add_u32 s6, s8, s6
	s_addc_u32 s7, s9, 0
	s_lshl_b32 s8, s11, 2
	s_add_u32 s6, s6, s8
	s_addc_u32 s7, s7, 0
	s_lshl_b32 s8, s11, 8
	s_add_u32 s0, s0, s8
	s_addc_u32 s1, s1, 0
	s_lshl_b32 s8, s10, 1
	s_add_u32 s0, s0, s8
	s_addc_u32 s1, s1, 0
	s_add_u32 s0, s0, 0x11580000
	s_addc_u32 s1, s1, 0
	s_mov_b64 s[8:9], 0
	s_branch .LBB0_26

; __device__ __forceinline__ CvtD cvt_decode(Frame& F, int it) {
;     ...
;     if (r < 2 * CI_P1) { const int kv = r / CI_P1; r -= kv * CI_P1; const int kb = r / 4, nb = r % 4;
;         return cvt_desc(inp(F, I_PW1) + ((size_t)l * 2 + kv) * 2048 * 128, 128, 64 * kb, 32 * nb, (bf16*)(lwp + LW_PHI1) + (size_t)kv * 128 * 2048, 2048, 32 * nb); }
.LBB0_26:
	s_andn2_b64 vcc, exec, s[8:9]
	s_cbranch_vccnz .LBB0_28
	s_add_i32 s0, 0, 0x23168
	v_mov_b32_e32 v0, s0
	ds_read_b64 v[0:1], v0
	s_add_i32 s8, s20, 0xfffeecc0
	s_lshr_b32 s0, s8, 7
	s_lshl_b64 s[6:7], s[4:5], 21
	s_mov_b32 s1, 0
	s_waitcnt lgkmcnt(0)
	v_readfirstlane_b32 s9, v0
	v_readfirstlane_b32 s10, v1
	s_add_u32 s9, s9, s6
	s_addc_u32 s10, s10, s7
	s_lshl_b64 s[6:7], s[0:1], 20
	s_add_u32 s6, s9, s6
	s_addc_u32 s7, s10, s7
	s_lshl_b32 s8, s8, 4
	s_lshl_b32 s9, s101, 5
	s_and_b32 s8, s8, 0x7c0
	s_and_b32 s9, s9, 0x60
	s_lshl_b64 s[0:1], s[0:1], 19
	s_add_u32 s0, s18, s0
	s_addc_u32 s1, s19, s1
	s_lshl_b32 s10, s8, 9
	s_add_u32 s6, s6, s10
	s_addc_u32 s7, s7, 0
	s_lshl_b32 s10, s9, 2
	s_add_u32 s6, s6, s10
	s_addc_u32 s7, s7, 0
	s_lshl_b32 s9, s9, 12
	s_add_u32 s0, s0, s9
	s_addc_u32 s1, s1, 0
	s_lshl_b32 s8, s8, 1
	s_add_u32 s0, s0, s8
	s_addc_u32 s1, s1, 0
	s_add_u32 s0, s0, 0x11480000
	s_addc_u32 s1, s1, 0
	s_mov_b64 s[8:9], 0x80
	s_movk_i32 s24, 0x800
	s_branch .LBB0_29

; #define GAS __attribute__((address_space(1)))
; #define LAS __attribute__((address_space(3)))
; #define LDS_WAIT() asm volatile("s_waitcnt lgkmcnt(0)" ::: "memory")
; __device__ __forceinline__ unsigned pk2(float lo, float hi) { unsigned r; asm("v_cvt_pk_bf16_f32 %0, %1, %2" : "=v"(r) : "v"(lo), "v"(hi)); return r; }
; __device__ __forceinline__ void cvt_load(const CvtD& d, f32x4 (&v)[8], int lane) {
;     const float* src = d.src + (size_t)(lane >> 3) * d.ldw + 4 * (lane & 7);
; #pragma unroll
;     for (int i = 0; i < 8; ++i) v[i] = *(const f32x4*)(src + (size_t)(8 * i) * d.ldw);
; }
; __device__ __forceinline__ void cvt_store(const CvtD& d, const f32x4 (&v)[8], LAS float* scr, int lane) {
; #pragma unroll
;     for (int i = 0; i < 8; ++i) { LAS float* p = scr + (8 * i + (lane >> 3)) * 33 + 4 * (lane & 7); p[0] = v[i][0]; p[1] = v[i][1]; p[2] = v[i][2]; p[3] = v[i][3]; }
;     LDS_WAIT(); asm volatile("" ::: "memory");
;     const int c = lane & 7;
; #pragma unroll
;     for (int j = 0; j < 4; ++j) { const int n = (lane >> 3) + 8 * j; const LAS float* sp = scr + (8 * c) * 33 + n;
;         u32x4 o; o.x = pk2(sp[0 * 33], sp[1 * 33]); o.y = pk2(sp[2 * 33], sp[3 * 33]); o.z = pk2(sp[4 * 33], sp[5 * 33]); o.w = pk2(sp[6 * 33], sp[7 * 33]);
;         *(GAS u32x4*)(d.dst + (size_t)n * d.K + 8 * c) = o; }
; __device__ __forceinline__ void p0_prologue(const Args& a, Frame& F) {
;     ...
;     { int it = gw;
;         if (it < DEPTH * CI_PER_LAYER) { CvtD d = cvt_decode(F, it); f32x4 v[8]; cvt_load(d, v, F.lane);
;             for (;;) { const int itn = it + NGW; const bool more = itn < DEPTH * CI_PER_LAYER; CvtD dn = d; f32x4 vn[8];
;                 if (more) { dn = cvt_decode(F, itn); cvt_load(dn, vn, F.lane); }
.LBB0_53:
	v_bfe_u32 v66, v64, 3, 3
	v_mul_u32_u24_e32 v0, s8, v66
	v_lshlrev_b32_e32 v2, 2, v64
	v_mov_b32_e32 v69, 0
	v_lshlrev_b32_e32 v68, 2, v0
	v_and_b32_e32 v32, 28, v2
	v_lshl_add_u64 v[0:1], s[6:7], 0, v[68:69]
	v_lshlrev_b32_e32 v68, 2, v32
	v_lshl_add_u64 v[0:1], v[0:1], 0, v[68:69]
	s_lshl_b64 s[4:5], s[8:9], 5
	v_lshl_add_u64 v[2:3], v[0:1], 0, s[4:5]
	flat_load_dwordx4 v[28:31], v[0:1]
	flat_load_dwordx4 v[24:27], v[2:3]
	v_lshl_add_u64 v[0:1], v[2:3], 0, s[4:5]
	v_lshl_add_u64 v[2:3], v[0:1], 0, s[4:5]
	flat_load_dwordx4 v[20:23], v[0:1]
	flat_load_dwordx4 v[16:19], v[2:3]
	v_lshl_add_u64 v[0:1], v[2:3], 0, s[4:5]
	v_lshl_add_u64 v[2:3], v[0:1], 0, s[4:5]
	v_lshl_add_u64 v[34:35], v[2:3], 0, s[4:5]
	flat_load_dwordx4 v[12:15], v[0:1]
	flat_load_dwordx4 v[8:11], v[2:3]
	v_lshl_add_u64 v[36:37], v[34:35], 0, s[4:5]
	flat_load_dwordx4 v[4:7], v[34:35]
	flat_load_dwordx4 v[0:3], v[36:37]
	v_lshlrev_b32_e32 v34, 3, v64
	s_lshl_b32 s4, s13, 14
	v_and_b32_e32 v34, 56, v34
	s_add_i32 s4, s4, 0
	v_mul_u32_u24_e32 v36, 0x84, v34
	v_lshlrev_b32_e32 v37, 2, v66
	s_lshl_b32 s25, s52, 3
	v_add_u32_e32 v33, s4, v68
	v_add3_u32 v65, s4, v36, v37
	s_lshl_b32 s4, s92, 8
	s_lshl_b32 s6, s13, 5
	s_lshl_b32 s26, s101, 5
	s_add_i32 s4, s13, s25
	s_add_i32 s30, s4, s12
	v_mul_u32_u24_e32 v35, 0x84, v66
	s_lshl_b32 s4, s30, 4
	s_mov_b32 s5, 0
	v_or_b32_e32 v70, 8, v66
	v_or_b32_e32 v72, 16, v66
	v_or_b32_e32 v74, 24, v66
	s_lshl_b32 s27, s52, 8
	s_add_i32 s31, s4, 0xffeecc00
	s_lshl_b32 s34, s52, 7
	s_lshl_b32 s35, s30, 6
	s_lshl_b32 s36, s52, 9
	s_add_i32 s37, 0, 0x23178
	s_add_i32 s38, 0, 0x23168
	s_add_i32 s39, 0, 0x231c0
	s_add_i32 s40, 0, 0x231c8
	s_add_i32 s41, 0, 0x231b8
	s_add_i32 s42, 0, 0x231b0
	s_add_i32 s43, 0, 0x23188
	s_add_i32 s44, 0, 0x23180
	s_add_i32 s45, 0, 0x23110
	v_lshlrev_b32_e32 v76, 2, v32
	v_add_u32_e32 v67, v33, v35
	v_lshlrev_b32_e32 v78, 1, v34
	s_mov_b64 s[8:9], s[0:1]
	s_mov_b32 s4, s24
	s_branch .LBB0_55
